# speedup vs baseline: 1.0768x; 1.0768x over previous
.LBB2_6:
	s_or_b64 exec, exec, s[18:19]
	v_xor_b32_e32 v23, 32, v23
	s_add_i32 s38, 0, 0x1c000
	v_lshlrev_b32_e32 v23, 2, v23
	v_lshlrev_b32_e32 v199, 2, v25
	s_waitcnt vmcnt(4) lgkmcnt(0)
	s_barrier
	v_add3_u32 v23, s38, v23, v199
	ds_read_b32 v23, v23
	v_max_f32_e32 v24, v24, v24
	v_mul_f32_e32 v22, 0x3db8aa3b, v22
	v_mov_b32_e32 v164, 0
	v_mov_b32_e32 v165, 0
	s_waitcnt lgkmcnt(0)
	s_movk_i32 s45, 0x4000
	v_add3_u32 v250, s45, v184, v185
	v_add3_u32 v251, s45, v184, v186
	v_add3_u32 v252, s45, v184, v187
	v_add3_u32 v253, s45, v184, v188
	ds_read_b128 v[218:221], v250 offset:49152
	ds_read_b128 v[222:225], v251 offset:49152
	ds_read_b128 v[242:245], v252 offset:49152
	ds_read_b128 v[246:249], v253 offset:49152
	v_add3_u32 v250, s45, v184, v189
	v_add3_u32 v251, s45, v184, v190
	v_add3_u32 v252, s45, v184, v191
	v_add3_u32 v253, s45, v184, v192
	ds_read_b128 v[202:205], v250 offset:49152
	ds_read_b128 v[206:209], v251 offset:49152
	ds_read_b128 v[210:213], v252 offset:49152
	ds_read_b128 v[214:217], v253 offset:49152
	v_max_f32_e32 v23, v23, v23
	v_max_f32_e32 v197, v24, v23
	v_mov_b32_e32 v23, 2.0
	v_fmamk_f32 v200, v197, 0xbdb8aa3b, v23
	v_fmamk_f32 v23, v22, 0xcb400000, v200
	v_fma_f32 v2, v2, v22, v23
	v_fma_f32 v3, v3, v22, v23
	v_fma_f32 v6, v6, v22, v23
	v_fma_f32 v7, v7, v22, v23
	v_fma_f32 v10, v10, v22, v23
	v_fma_f32 v11, v11, v22, v23
	v_fma_f32 v14, v14, v22, v23
	v_fma_f32 v15, v15, v22, v23
	v_exp_f32_e32 v2, v2
	v_exp_f32_e32 v3, v3
	v_exp_f32_e32 v6, v6
	v_exp_f32_e32 v7, v7
	v_exp_f32_e32 v10, v10
	v_exp_f32_e32 v11, v11
	v_exp_f32_e32 v14, v14
	v_exp_f32_e32 v15, v15
	v_fma_f32 v4, v4, v22, v23
	v_fma_f32 v5, v5, v22, v23
	v_fma_f32 v8, v8, v22, v23
	v_fma_f32 v9, v9, v22, v23
	v_fma_f32 v12, v12, v22, v23
	v_fma_f32 v13, v13, v22, v23
	v_fma_f32 v16, v16, v22, v23
	v_fmac_f32_e32 v23, v17, v22
	v_mov_b32_e32 v166, 0
	v_mov_b32_e32 v167, 0
	v_exp_f32_e32 v4, v4
	v_exp_f32_e32 v5, v5
	v_exp_f32_e32 v8, v8
	v_exp_f32_e32 v9, v9
	v_exp_f32_e32 v12, v12
	v_exp_f32_e32 v13, v13
	v_exp_f32_e32 v16, v16
	v_exp_f32_e32 v17, v23
	v_cvt_pk_fp8_f32 v164, v2, v3
	v_cvt_pk_fp8_f32 v165, v6, v7
	v_cvt_pk_fp8_f32 v166, v10, v11
	v_cvt_pk_fp8_f32 v167, v14, v15
	s_lshl_b32 s0, s22, 11
	s_add_i32 s0, s0, 0
	s_add_i32 s0, s0, 0x18000
	v_cvt_pk_fp8_f32 v164, v4, v5 op_sel:[0,0,1]
	v_cvt_pk_fp8_f32 v165, v8, v9 op_sel:[0,0,1]
	v_cvt_pk_fp8_f32 v166, v12, v13 op_sel:[0,0,1]
	v_cvt_pk_fp8_f32 v167, v16, v17 op_sel:[0,0,1]
	v_lshl_add_u32 v193, v198, 5, s0
	v_lshrrev_b32_e32 v3, 2, v0
	v_lshlrev_b32_e32 v6, 1, v183
	s_lshl_b32 s0, s20, 20
	v_bfe_u32 v4, v0, 2, 2
	v_lshl_or_b32 v5, v1, 6, s24
	v_bitop3_b32 v3, v6, v3, 3 bitop3:0x78
	s_or_b32 s18, s0, s23
	v_lshl_add_u32 v194, s34, 4, v193
	v_lshl_or_b32 v195, v3, 4, v5
	v_bitop3_b32 v3, v6, v4, 1 bitop3:0x36
	v_add3_u32 v4, s21, v20, v21
	s_add_u32 s0, s6, s18
	ds_write_b128 v194, v[164:167]
	v_lshl_or_b32 v196, v3, 4, v5
	v_ashrrev_i32_e32 v5, 31, v4
	s_addc_u32 s1, s7, 0
	s_waitcnt vmcnt(2) lgkmcnt(0)
	s_barrier
	s_mov_b64 s[60:61], s[0:1]
	v_lshl_add_u64 v[170:171], s[0:1], 0, v[4:5]
	v_add3_u32 v4, s21, v18, v19
	s_add_u32 s0, s8, s18
	v_mov_b32_e32 v2, 0
	v_ashrrev_i32_e32 v5, 31, v4
	s_addc_u32 s1, s9, 0
	s_mov_b32 s39, 0
	s_mov_b32 s40, 1
	s_mov_b64 s[64:65], s[0:1]
	v_lshl_add_u64 v[172:173], s[0:1], 0, v[4:5]
	s_mov_b64 s[6:7], 0
	s_movk_i32 s41, 0x2000
	s_mov_b64 s[8:9], 0xc000
	s_mov_b64 s[18:19], 0xe000
	s_mov_b64 s[20:21], 0x8000
	s_mov_b64 s[22:23], 0xa000
	s_mov_b32 s42, 0x42966666
	v_mov_b32_e32 v82, 0x4b400000
	v_mov_b32_e32 v100, 0x38383838
	s_mov_b32 s0, 0
	s_mov_b32 s43, 1
	v_mov_b32_e32 v3, v2
	v_mov_b32_e32 v4, v2
	v_mov_b32_e32 v5, v2
	v_mov_b32_e32 v6, v2
	v_mov_b32_e32 v7, v2
	v_mov_b32_e32 v8, v2
	v_mov_b32_e32 v9, v2
	v_mov_b32_e32 v10, v2
	v_mov_b32_e32 v11, v2
	v_mov_b32_e32 v12, v2
	v_mov_b32_e32 v13, v2
	v_mov_b32_e32 v14, v2
	v_mov_b32_e32 v15, v2
	v_mov_b32_e32 v16, v2
	v_mov_b32_e32 v17, v2
	v_mov_b32_e32 v18, v2
	v_mov_b32_e32 v19, v2
	v_mov_b32_e32 v20, v2
	v_mov_b32_e32 v21, v2
	v_mov_b32_e32 v22, v2
	v_mov_b32_e32 v23, v2
	v_mov_b32_e32 v24, v2
	v_mov_b32_e32 v25, v2
	v_mov_b32_e32 v26, v2
	v_mov_b32_e32 v27, v2
	v_mov_b32_e32 v28, v2
	v_mov_b32_e32 v29, v2
	v_mov_b32_e32 v30, v2
	v_mov_b32_e32 v31, v2
	v_mov_b32_e32 v32, v2
	v_mov_b32_e32 v33, v2
	v_mov_b32_e32 v34, v2
	v_mov_b32_e32 v35, v2
	v_mov_b32_e32 v36, v2
	v_mov_b32_e32 v37, v2
	v_mov_b32_e32 v38, v2
	v_mov_b32_e32 v39, v2
	v_mov_b32_e32 v40, v2
	v_mov_b32_e32 v41, v2
	v_mov_b32_e32 v42, v2
	v_mov_b32_e32 v43, v2
	v_mov_b32_e32 v44, v2
	v_mov_b32_e32 v45, v2
	v_mov_b32_e32 v46, v2
	v_mov_b32_e32 v47, v2
	v_mov_b32_e32 v48, v2
	v_mov_b32_e32 v49, v2
	v_mov_b32_e32 v50, v2
	v_mov_b32_e32 v51, v2
	v_mov_b32_e32 v52, v2
	v_mov_b32_e32 v53, v2
	v_mov_b32_e32 v54, v2
	v_mov_b32_e32 v55, v2
	v_mov_b32_e32 v56, v2
	v_mov_b32_e32 v57, v2
	v_mov_b32_e32 v58, v2
	v_mov_b32_e32 v59, v2
	v_mov_b32_e32 v60, v2
	v_mov_b32_e32 v61, v2
	v_mov_b32_e32 v62, v2
	v_mov_b32_e32 v63, v2
	v_mov_b32_e32 v64, v2
	v_mov_b32_e32 v65, v2
	v_mov_b32_e32 v66, v2
	v_mov_b32_e32 v67, v2
	v_mov_b32_e32 v68, v2
	v_mov_b32_e32 v69, v2
	v_mov_b32_e32 v70, v2
	v_mov_b32_e32 v71, v2
	v_mov_b32_e32 v72, v2
	v_mov_b32_e32 v73, v2
	v_mov_b32_e32 v74, v2
	v_mov_b32_e32 v75, v2
	v_mov_b32_e32 v76, v2
	v_mov_b32_e32 v77, v2
	v_mov_b32_e32 v78, v2
	v_mov_b32_e32 v79, v2
	v_mov_b32_e32 v80, v2
	v_mov_b32_e32 v81, v2
	v_mov_b32_e32 v101, v100
	v_mov_b32_e32 v102, v100
	v_mov_b32_e32 v103, v100
	v_mov_b32_e32 v104, v100
	v_mov_b32_e32 v105, v100
	v_mov_b32_e32 v106, v100
	v_mov_b32_e32 v107, v100
	v_mov_b32_e32 v226, 0x4b400000
	v_mov_b32_e32 v227, v226
	v_mov_b32_e32 v228, v226
	v_mov_b32_e32 v229, v226
	v_mov_b32_e32 v230, v226
	v_mov_b32_e32 v231, v226
	v_mov_b32_e32 v232, v226
	v_mov_b32_e32 v233, v226
	v_mov_b32_e32 v234, v226
	v_mov_b32_e32 v235, v226
	v_mov_b32_e32 v236, v226
	v_mov_b32_e32 v237, v226
	v_mov_b32_e32 v238, v226
	v_mov_b32_e32 v239, v226
	v_mov_b32_e32 v240, v226
	v_mov_b32_e32 v241, v226
	v_add_u32_e32 v250, 0xc000, v184
	v_add_u32_e32 v185, v185, v250
	v_add_u32_e32 v186, v186, v250
	v_add_u32_e32 v187, v187, v250
	v_add_u32_e32 v188, v188, v250
	v_add_u32_e32 v189, v189, v250
	v_add_u32_e32 v190, v190, v250
	v_add_u32_e32 v191, v191, v250
	v_add_u32_e32 v192, v192, v250
	v_subrev_u32_e32 v252, s60, v170
	v_subrev_u32_e32 v255, s64, v172
	v_add_u32_e32 v254, 0x2000, v252
	v_add_u32_e32 v201, 0x2000, v255
	s_add_u32 s60, s60, 0xc000
	s_addc_u32 s61, s61, 0
	s_add_u32 s64, s64, 0x8000
	s_addc_u32 s65, s65, 0
	v_mfma_i32_32x32x32_i8 v[84:99], v[218:221], v[132:135], v[226:241]
	v_mfma_i32_32x32x32_i8 v[84:99], v[222:225], v[136:139], v[84:99]
.Lat_u0:
	ds_read_b128 v[108:111], v193
	ds_read_b128 v[112:115], v193 offset:16
	v_mfma_i32_32x32x32_i8 v[84:99], v[242:245], v[140:143], v[84:99]
	ds_read_b128 v[116:119], v195 offset:6144
	ds_read_b128 v[120:123], v196 offset:6144
	s_cmp_gt_u32 s43, 29
	s_cbranch_scc1 .Lat_nok0
	s_add_i32 m0, s31, 49152
	s_nop 0
	global_load_lds_dwordx4 v252, s[60:61]
	s_add_i32 m0, s31, 57344
	v_mfma_i32_32x32x32_i8 v[84:99], v[246:249], v[144:147], v[84:99]
	global_load_lds_dwordx4 v254, s[60:61]
	s_branch .Lat_k0
.Lat_nok0:
	v_mfma_i32_32x32x32_i8 v[84:99], v[246:249], v[144:147], v[84:99]
.Lat_k0:
	ds_read_b128 v[124:127], v195 offset:4096
	ds_read_b128 v[128:131], v196 offset:4096
	v_mfma_i32_32x32x32_i8 v[84:99], v[202:205], v[148:151], v[84:99]
	ds_read_b128 v[202:205], v195
	v_mfma_i32_32x32x32_i8 v[84:99], v[206:209], v[152:155], v[84:99]
	ds_read_b128 v[206:209], v196
	v_mfma_i32_32x32x32_i8 v[84:99], v[210:213], v[156:159], v[84:99]
	ds_read_b128 v[210:213], v195 offset:2048
	v_mfma_i32_32x32x32_i8 v[84:99], v[214:217], v[160:163], v[84:99]
	ds_read_b128 v[214:217], v196 offset:2048
	v_readlane_b32 s50, v182, s43
	s_waitcnt lgkmcnt(6)
	v_mfma_f32_32x32x64_f8f6f4 v[2:17], v[108:115], v[116:123], v[2:17]
	ds_read_b128 v[218:221], v185 offset:32768
	ds_read_b128 v[222:225], v186 offset:32768
	ds_read_b128 v[242:245], v187 offset:32768
	ds_read_b128 v[246:249], v188 offset:32768
	v_mul_f32_e32 v82, s50, v168
	v_mul_f32_e32 v250, 0x3db8aa3b, v82
	v_fmamk_f32 v251, v250, 0xcb400000, v200
	s_cmp_gt_u32 s43, 30
	s_cbranch_scc1 .Lat_nov0
	s_add_i32 m0, s31, 32768
	v_max_i32_e32 v83, v84, v85
	global_load_lds_dwordx4 v255, s[64:65]
	s_add_i32 m0, s31, 40960
	v_max3_i32 v83, v83, v86, v87
	global_load_lds_dwordx4 v201, s[64:65]
	s_branch .Lat_v0
.Lat_nov0:
	v_max_i32_e32 v83, v84, v85
	v_max3_i32 v83, v83, v86, v87
.Lat_v0:
	v_max3_i32 v83, v83, v88, v89
	v_max3_i32 v83, v83, v90, v91
	v_max3_i32 v83, v83, v92, v93
	v_max3_i32 v83, v83, v94, v95
	v_max3_i32 v83, v83, v96, v97
	v_max3_i32 v83, v83, v98, v99
	s_waitcnt lgkmcnt(8)
	v_mfma_f32_32x32x64_f8f6f4 v[18:33], v[108:115], v[124:131], v[18:33]
	v_mov_b32_e32 v253, v83
	v_fma_f32 v84, v84, v250, v251
	v_fma_f32 v85, v85, v250, v251
	v_permlane32_swap_b32_e32 v83, v253
	v_fma_f32 v86, v86, v250, v251
	v_fma_f32 v87, v87, v250, v251
	v_max_i32_e32 v83, v83, v253
	v_exp_f32_e32 v84, v84
	v_exp_f32_e32 v85, v85
	v_add_f32_e32 v83, 0xcb400000, v83
	v_exp_f32_e32 v86, v86
	v_exp_f32_e32 v87, v87
	v_fma_f32 v82, v82, v83, -v197
	v_fma_f32 v88, v88, v250, v251
	v_fma_f32 v89, v89, v250, v251
	v_fma_f32 v90, v90, v250, v251
	v_fma_f32 v91, v91, v250, v251
	v_mfma_f32_32x32x64_f8f6f4 v[66:81], v[108:115], v[100:107], v[66:81]
	v_cmp_ge_f32_e64 s[52:53], s42, v82
	v_cvt_pk_fp8_f32 v164, v84, v85
	v_cvt_pk_fp8_f32 v164, v86, v87 op_sel:[0,0,1]
	v_exp_f32_e32 v88, v88
	v_exp_f32_e32 v89, v89
	v_exp_f32_e32 v90, v90
	v_exp_f32_e32 v91, v91
	v_fma_f32 v92, v92, v250, v251
	v_fma_f32 v93, v93, v250, v251
	v_fma_f32 v94, v94, v250, v251
	v_fma_f32 v95, v95, v250, v251
	v_cvt_pk_fp8_f32 v165, v88, v89
	v_cvt_pk_fp8_f32 v165, v90, v91 op_sel:[0,0,1]
	v_exp_f32_e32 v92, v92
	v_exp_f32_e32 v93, v93
	v_exp_f32_e32 v94, v94
	v_exp_f32_e32 v95, v95
	s_waitcnt lgkmcnt(6)
	v_mfma_f32_32x32x64_f8f6f4 v[50:65], v[108:115], v[202:209], v[50:65]
	ds_read_b128 v[202:205], v189 offset:32768
	ds_read_b128 v[206:209], v190 offset:32768
	v_fma_f32 v96, v96, v250, v251
	v_fma_f32 v97, v97, v250, v251
	v_fma_f32 v98, v98, v250, v251
	v_fma_f32 v99, v99, v250, v251
	v_cvt_pk_fp8_f32 v166, v92, v93
	v_cvt_pk_fp8_f32 v166, v94, v95 op_sel:[0,0,1]
	v_exp_f32_e32 v96, v96
	v_exp_f32_e32 v97, v97
	v_exp_f32_e32 v98, v98
	v_exp_f32_e32 v99, v99
	s_cmp_lg_u64 s[52:53], exec
	s_cselect_b32 s1, 1, 0
	s_or_b32 s39, s39, s1
	v_cvt_pk_fp8_f32 v167, v96, v97
	v_cvt_pk_fp8_f32 v167, v98, v99 op_sel:[0,0,1]
	ds_write_b128 v194, v[164:167] offset:8192
	s_waitcnt lgkmcnt(7)
	v_mfma_f32_32x32x64_f8f6f4 v[34:49], v[108:115], v[210:217], v[34:49]
	ds_read_b128 v[210:213], v191 offset:32768
	ds_read_b128 v[214:217], v192 offset:32768
	s_add_u32 s60, s60, 0x4000
	s_addc_u32 s61, s61, 0
	s_add_u32 s64, s64, 0x4000
	s_addc_u32 s65, s65, 0
	s_add_i32 s43, s43, 1
	s_cmp_eq_u32 s43, 32
	s_cbranch_scc1 .Lat_last
	s_waitcnt lgkmcnt(7)
	v_mfma_i32_32x32x32_i8 v[84:99], v[218:221], v[132:135], v[226:241]
	v_mfma_i32_32x32x32_i8 v[84:99], v[222:225], v[136:139], v[84:99]
	s_waitcnt vmcnt(2) lgkmcnt(0)
	s_barrier
.Lat_u1:
	ds_read_b128 v[108:111], v193 offset:8192
	ds_read_b128 v[112:115], v193 offset:8208
	v_mfma_i32_32x32x32_i8 v[84:99], v[242:245], v[140:143], v[84:99]
	ds_read_b128 v[116:119], v195 offset:22528
	ds_read_b128 v[120:123], v196 offset:22528
	s_add_i32 m0, s31, 65536
	s_nop 0
	global_load_lds_dwordx4 v252, s[60:61]
	s_add_i32 m0, s31, 73728
	v_mfma_i32_32x32x32_i8 v[84:99], v[246:249], v[144:147], v[84:99]
	global_load_lds_dwordx4 v254, s[60:61]
	ds_read_b128 v[124:127], v195 offset:20480
	ds_read_b128 v[128:131], v196 offset:20480
	v_mfma_i32_32x32x32_i8 v[84:99], v[202:205], v[148:151], v[84:99]
	ds_read_b128 v[202:205], v195 offset:16384
	v_mfma_i32_32x32x32_i8 v[84:99], v[206:209], v[152:155], v[84:99]
	ds_read_b128 v[206:209], v196 offset:16384
	v_mfma_i32_32x32x32_i8 v[84:99], v[210:213], v[156:159], v[84:99]
	ds_read_b128 v[210:213], v195 offset:18432
	v_mfma_i32_32x32x32_i8 v[84:99], v[214:217], v[160:163], v[84:99]
	ds_read_b128 v[214:217], v196 offset:18432
	v_readlane_b32 s50, v182, s43
	s_waitcnt lgkmcnt(6)
	v_mfma_f32_32x32x64_f8f6f4 v[2:17], v[108:115], v[116:123], v[2:17]
	ds_read_b128 v[218:221], v185
	ds_read_b128 v[222:225], v186
	ds_read_b128 v[242:245], v187
	ds_read_b128 v[246:249], v188
	v_mul_f32_e32 v82, s50, v168
	v_mul_f32_e32 v250, 0x3db8aa3b, v82
	v_fmamk_f32 v251, v250, 0xcb400000, v200
	s_mov_b32 m0, s31
	v_max_i32_e32 v83, v84, v85
	global_load_lds_dwordx4 v255, s[64:65]
	s_add_i32 m0, s31, 8192
	v_max3_i32 v83, v83, v86, v87
	global_load_lds_dwordx4 v201, s[64:65]
	v_max3_i32 v83, v83, v88, v89
	v_max3_i32 v83, v83, v90, v91
	v_max3_i32 v83, v83, v92, v93
	v_max3_i32 v83, v83, v94, v95
	v_max3_i32 v83, v83, v96, v97
	v_max3_i32 v83, v83, v98, v99
	s_waitcnt lgkmcnt(8)
	v_mfma_f32_32x32x64_f8f6f4 v[18:33], v[108:115], v[124:131], v[18:33]
	v_mov_b32_e32 v253, v83
	v_fma_f32 v84, v84, v250, v251
	v_fma_f32 v85, v85, v250, v251
	v_permlane32_swap_b32_e32 v83, v253
	v_fma_f32 v86, v86, v250, v251
	v_fma_f32 v87, v87, v250, v251
	v_max_i32_e32 v83, v83, v253
	v_exp_f32_e32 v84, v84
	v_exp_f32_e32 v85, v85
	v_add_f32_e32 v83, 0xcb400000, v83
	v_exp_f32_e32 v86, v86
	v_exp_f32_e32 v87, v87
	v_fma_f32 v82, v82, v83, -v197
	v_fma_f32 v88, v88, v250, v251
	v_fma_f32 v89, v89, v250, v251
	v_fma_f32 v90, v90, v250, v251
	v_fma_f32 v91, v91, v250, v251
	v_mfma_f32_32x32x64_f8f6f4 v[66:81], v[108:115], v[100:107], v[66:81]
	v_cmp_ge_f32_e64 s[52:53], s42, v82
	v_cvt_pk_fp8_f32 v164, v84, v85
	v_cvt_pk_fp8_f32 v164, v86, v87 op_sel:[0,0,1]
	v_exp_f32_e32 v88, v88
	v_exp_f32_e32 v89, v89
	v_exp_f32_e32 v90, v90
	v_exp_f32_e32 v91, v91
	v_fma_f32 v92, v92, v250, v251
	v_fma_f32 v93, v93, v250, v251
	v_fma_f32 v94, v94, v250, v251
	v_fma_f32 v95, v95, v250, v251
	v_cvt_pk_fp8_f32 v165, v88, v89
	v_cvt_pk_fp8_f32 v165, v90, v91 op_sel:[0,0,1]
	v_exp_f32_e32 v92, v92
	v_exp_f32_e32 v93, v93
	v_exp_f32_e32 v94, v94
	v_exp_f32_e32 v95, v95
	s_waitcnt lgkmcnt(6)
	v_mfma_f32_32x32x64_f8f6f4 v[50:65], v[108:115], v[202:209], v[50:65]
	ds_read_b128 v[202:205], v189
	ds_read_b128 v[206:209], v190
	v_fma_f32 v96, v96, v250, v251
	v_fma_f32 v97, v97, v250, v251
	v_fma_f32 v98, v98, v250, v251
	v_fma_f32 v99, v99, v250, v251
	v_cvt_pk_fp8_f32 v166, v92, v93
	v_cvt_pk_fp8_f32 v166, v94, v95 op_sel:[0,0,1]
	v_exp_f32_e32 v96, v96
	v_exp_f32_e32 v97, v97
	v_exp_f32_e32 v98, v98
	v_exp_f32_e32 v99, v99
	s_cmp_lg_u64 s[52:53], exec
	s_cselect_b32 s1, 1, 0
	s_or_b32 s39, s39, s1
	v_cvt_pk_fp8_f32 v167, v96, v97
	v_cvt_pk_fp8_f32 v167, v98, v99 op_sel:[0,0,1]
	ds_write_b128 v194, v[164:167]
	s_waitcnt lgkmcnt(7)
	v_mfma_f32_32x32x64_f8f6f4 v[34:49], v[108:115], v[210:217], v[34:49]
	ds_read_b128 v[210:213], v191
	ds_read_b128 v[214:217], v192
	s_add_u32 s60, s60, 0x4000
	s_addc_u32 s61, s61, 0
	s_add_u32 s64, s64, 0x4000
	s_addc_u32 s65, s65, 0
	s_add_i32 s43, s43, 1
	s_waitcnt lgkmcnt(7)
	v_mfma_i32_32x32x32_i8 v[84:99], v[218:221], v[132:135], v[226:241]
	v_mfma_i32_32x32x32_i8 v[84:99], v[222:225], v[136:139], v[84:99]
	s_waitcnt vmcnt(2) lgkmcnt(0)
	s_barrier
.Lat_u2:
	ds_read_b128 v[108:111], v193
	ds_read_b128 v[112:115], v193 offset:16
	v_mfma_i32_32x32x32_i8 v[84:99], v[242:245], v[140:143], v[84:99]
	ds_read_b128 v[116:119], v195 offset:38912
	ds_read_b128 v[120:123], v196 offset:38912
	s_add_i32 m0, s31, 81920
	s_nop 0
	global_load_lds_dwordx4 v252, s[60:61]
	s_add_i32 m0, s31, 90112
	v_mfma_i32_32x32x32_i8 v[84:99], v[246:249], v[144:147], v[84:99]
	global_load_lds_dwordx4 v254, s[60:61]
	ds_read_b128 v[124:127], v195 offset:36864
	ds_read_b128 v[128:131], v196 offset:36864
	v_mfma_i32_32x32x32_i8 v[84:99], v[202:205], v[148:151], v[84:99]
	ds_read_b128 v[202:205], v195 offset:32768
	v_mfma_i32_32x32x32_i8 v[84:99], v[206:209], v[152:155], v[84:99]
	ds_read_b128 v[206:209], v196 offset:32768
	v_mfma_i32_32x32x32_i8 v[84:99], v[210:213], v[156:159], v[84:99]
	ds_read_b128 v[210:213], v195 offset:34816
	v_mfma_i32_32x32x32_i8 v[84:99], v[214:217], v[160:163], v[84:99]
	ds_read_b128 v[214:217], v196 offset:34816
	v_readlane_b32 s50, v182, s43
	s_waitcnt lgkmcnt(6)
	v_mfma_f32_32x32x64_f8f6f4 v[2:17], v[108:115], v[116:123], v[2:17]
	ds_read_b128 v[218:221], v185 offset:16384
	ds_read_b128 v[222:225], v186 offset:16384
	ds_read_b128 v[242:245], v187 offset:16384
	ds_read_b128 v[246:249], v188 offset:16384
	v_mul_f32_e32 v82, s50, v168
	v_mul_f32_e32 v250, 0x3db8aa3b, v82
	v_fmamk_f32 v251, v250, 0xcb400000, v200
	s_add_i32 m0, s31, 16384
	v_max_i32_e32 v83, v84, v85
	global_load_lds_dwordx4 v255, s[64:65]
	s_add_i32 m0, s31, 24576
	v_max3_i32 v83, v83, v86, v87
	global_load_lds_dwordx4 v201, s[64:65]
	v_max3_i32 v83, v83, v88, v89
	v_max3_i32 v83, v83, v90, v91
	v_max3_i32 v83, v83, v92, v93
	v_max3_i32 v83, v83, v94, v95
	v_max3_i32 v83, v83, v96, v97
	v_max3_i32 v83, v83, v98, v99
	s_waitcnt lgkmcnt(8)
	v_mfma_f32_32x32x64_f8f6f4 v[18:33], v[108:115], v[124:131], v[18:33]
	v_mov_b32_e32 v253, v83
	v_fma_f32 v84, v84, v250, v251
	v_fma_f32 v85, v85, v250, v251
	v_permlane32_swap_b32_e32 v83, v253
	v_fma_f32 v86, v86, v250, v251
	v_fma_f32 v87, v87, v250, v251
	v_max_i32_e32 v83, v83, v253
	v_exp_f32_e32 v84, v84
	v_exp_f32_e32 v85, v85
	v_add_f32_e32 v83, 0xcb400000, v83
	v_exp_f32_e32 v86, v86
	v_exp_f32_e32 v87, v87
	v_fma_f32 v82, v82, v83, -v197
	v_fma_f32 v88, v88, v250, v251
	v_fma_f32 v89, v89, v250, v251
	v_fma_f32 v90, v90, v250, v251
	v_fma_f32 v91, v91, v250, v251
	v_mfma_f32_32x32x64_f8f6f4 v[66:81], v[108:115], v[100:107], v[66:81]
	v_cmp_ge_f32_e64 s[52:53], s42, v82
	v_cvt_pk_fp8_f32 v164, v84, v85
	v_cvt_pk_fp8_f32 v164, v86, v87 op_sel:[0,0,1]
	v_exp_f32_e32 v88, v88
	v_exp_f32_e32 v89, v89
	v_exp_f32_e32 v90, v90
	v_exp_f32_e32 v91, v91
	v_fma_f32 v92, v92, v250, v251
	v_fma_f32 v93, v93, v250, v251
	v_fma_f32 v94, v94, v250, v251
	v_fma_f32 v95, v95, v250, v251
	v_cvt_pk_fp8_f32 v165, v88, v89
	v_cvt_pk_fp8_f32 v165, v90, v91 op_sel:[0,0,1]
	v_exp_f32_e32 v92, v92
	v_exp_f32_e32 v93, v93
	v_exp_f32_e32 v94, v94
	v_exp_f32_e32 v95, v95
	s_waitcnt lgkmcnt(6)
	v_mfma_f32_32x32x64_f8f6f4 v[50:65], v[108:115], v[202:209], v[50:65]
	ds_read_b128 v[202:205], v189 offset:16384
	ds_read_b128 v[206:209], v190 offset:16384
	v_fma_f32 v96, v96, v250, v251
	v_fma_f32 v97, v97, v250, v251
	v_fma_f32 v98, v98, v250, v251
	v_fma_f32 v99, v99, v250, v251
	v_cvt_pk_fp8_f32 v166, v92, v93
	v_cvt_pk_fp8_f32 v166, v94, v95 op_sel:[0,0,1]
	v_exp_f32_e32 v96, v96
	v_exp_f32_e32 v97, v97
	v_exp_f32_e32 v98, v98
	v_exp_f32_e32 v99, v99
	s_cmp_lg_u64 s[52:53], exec
	s_cselect_b32 s1, 1, 0
	s_or_b32 s39, s39, s1
	v_cvt_pk_fp8_f32 v167, v96, v97
	v_cvt_pk_fp8_f32 v167, v98, v99 op_sel:[0,0,1]
	ds_write_b128 v194, v[164:167] offset:8192
	s_waitcnt lgkmcnt(7)
	v_mfma_f32_32x32x64_f8f6f4 v[34:49], v[108:115], v[210:217], v[34:49]
	ds_read_b128 v[210:213], v191 offset:16384
	ds_read_b128 v[214:217], v192 offset:16384
	s_add_u32 s60, s60, 0x4000
	s_addc_u32 s61, s61, 0
	s_add_u32 s64, s64, 0x4000
	s_addc_u32 s65, s65, 0
	s_add_i32 s43, s43, 1
	s_waitcnt lgkmcnt(7)
	v_mfma_i32_32x32x32_i8 v[84:99], v[218:221], v[132:135], v[226:241]
	v_mfma_i32_32x32x32_i8 v[84:99], v[222:225], v[136:139], v[84:99]
	s_waitcnt vmcnt(2) lgkmcnt(0)
	s_barrier
.Lat_u3:
	ds_read_b128 v[108:111], v193 offset:8192
	ds_read_b128 v[112:115], v193 offset:8208
	v_mfma_i32_32x32x32_i8 v[84:99], v[242:245], v[140:143], v[84:99]
	ds_read_b128 v[116:119], v195 offset:6144
	ds_read_b128 v[120:123], v196 offset:6144
	s_add_i32 m0, s31, 49152
	s_nop 0
	global_load_lds_dwordx4 v252, s[60:61]
	s_add_i32 m0, s31, 57344
	v_mfma_i32_32x32x32_i8 v[84:99], v[246:249], v[144:147], v[84:99]
	global_load_lds_dwordx4 v254, s[60:61]
	ds_read_b128 v[124:127], v195 offset:4096
	ds_read_b128 v[128:131], v196 offset:4096
	v_mfma_i32_32x32x32_i8 v[84:99], v[202:205], v[148:151], v[84:99]
	ds_read_b128 v[202:205], v195
	v_mfma_i32_32x32x32_i8 v[84:99], v[206:209], v[152:155], v[84:99]
	ds_read_b128 v[206:209], v196
	v_mfma_i32_32x32x32_i8 v[84:99], v[210:213], v[156:159], v[84:99]
	ds_read_b128 v[210:213], v195 offset:2048
	v_mfma_i32_32x32x32_i8 v[84:99], v[214:217], v[160:163], v[84:99]
	ds_read_b128 v[214:217], v196 offset:2048
	v_readlane_b32 s50, v182, s43
	s_waitcnt lgkmcnt(6)
	v_mfma_f32_32x32x64_f8f6f4 v[2:17], v[108:115], v[116:123], v[2:17]
	ds_read_b128 v[218:221], v185 offset:32768
	ds_read_b128 v[222:225], v186 offset:32768
	ds_read_b128 v[242:245], v187 offset:32768
	ds_read_b128 v[246:249], v188 offset:32768
	v_mul_f32_e32 v82, s50, v168
	v_mul_f32_e32 v250, 0x3db8aa3b, v82
	v_fmamk_f32 v251, v250, 0xcb400000, v200
	s_add_i32 m0, s31, 32768
	v_max_i32_e32 v83, v84, v85
	global_load_lds_dwordx4 v255, s[64:65]
	s_add_i32 m0, s31, 40960
	v_max3_i32 v83, v83, v86, v87
	global_load_lds_dwordx4 v201, s[64:65]
	v_max3_i32 v83, v83, v88, v89
	v_max3_i32 v83, v83, v90, v91
	v_max3_i32 v83, v83, v92, v93
	v_max3_i32 v83, v83, v94, v95
	v_max3_i32 v83, v83, v96, v97
	v_max3_i32 v83, v83, v98, v99
	s_waitcnt lgkmcnt(8)
	v_mfma_f32_32x32x64_f8f6f4 v[18:33], v[108:115], v[124:131], v[18:33]
	v_mov_b32_e32 v253, v83
	v_fma_f32 v84, v84, v250, v251
	v_fma_f32 v85, v85, v250, v251
	v_permlane32_swap_b32_e32 v83, v253
	v_fma_f32 v86, v86, v250, v251
	v_fma_f32 v87, v87, v250, v251
	v_max_i32_e32 v83, v83, v253
	v_exp_f32_e32 v84, v84
	v_exp_f32_e32 v85, v85
	v_add_f32_e32 v83, 0xcb400000, v83
	v_exp_f32_e32 v86, v86
	v_exp_f32_e32 v87, v87
	v_fma_f32 v82, v82, v83, -v197
	v_fma_f32 v88, v88, v250, v251
	v_fma_f32 v89, v89, v250, v251
	v_fma_f32 v90, v90, v250, v251
	v_fma_f32 v91, v91, v250, v251
	v_mfma_f32_32x32x64_f8f6f4 v[66:81], v[108:115], v[100:107], v[66:81]
	v_cmp_ge_f32_e64 s[52:53], s42, v82
	v_cvt_pk_fp8_f32 v164, v84, v85
	v_cvt_pk_fp8_f32 v164, v86, v87 op_sel:[0,0,1]
	v_exp_f32_e32 v88, v88
	v_exp_f32_e32 v89, v89
	v_exp_f32_e32 v90, v90
	v_exp_f32_e32 v91, v91
	v_fma_f32 v92, v92, v250, v251
	v_fma_f32 v93, v93, v250, v251
	v_fma_f32 v94, v94, v250, v251
	v_fma_f32 v95, v95, v250, v251
	v_cvt_pk_fp8_f32 v165, v88, v89
	v_cvt_pk_fp8_f32 v165, v90, v91 op_sel:[0,0,1]
	v_exp_f32_e32 v92, v92
	v_exp_f32_e32 v93, v93
	v_exp_f32_e32 v94, v94
	v_exp_f32_e32 v95, v95
	s_waitcnt lgkmcnt(6)
	v_mfma_f32_32x32x64_f8f6f4 v[50:65], v[108:115], v[202:209], v[50:65]
	ds_read_b128 v[202:205], v189 offset:32768
	ds_read_b128 v[206:209], v190 offset:32768
	v_fma_f32 v96, v96, v250, v251
	v_fma_f32 v97, v97, v250, v251
	v_fma_f32 v98, v98, v250, v251
	v_fma_f32 v99, v99, v250, v251
	v_cvt_pk_fp8_f32 v166, v92, v93
	v_cvt_pk_fp8_f32 v166, v94, v95 op_sel:[0,0,1]
	v_exp_f32_e32 v96, v96
	v_exp_f32_e32 v97, v97
	v_exp_f32_e32 v98, v98
	v_exp_f32_e32 v99, v99
	s_cmp_lg_u64 s[52:53], exec
	s_cselect_b32 s1, 1, 0
	s_or_b32 s39, s39, s1
	v_cvt_pk_fp8_f32 v167, v96, v97
	v_cvt_pk_fp8_f32 v167, v98, v99 op_sel:[0,0,1]
	ds_write_b128 v194, v[164:167]
	s_waitcnt lgkmcnt(7)
	v_mfma_f32_32x32x64_f8f6f4 v[34:49], v[108:115], v[210:217], v[34:49]
	ds_read_b128 v[210:213], v191 offset:32768
	ds_read_b128 v[214:217], v192 offset:32768
	s_add_u32 s60, s60, 0x4000
	s_addc_u32 s61, s61, 0
	s_add_u32 s64, s64, 0x4000
	s_addc_u32 s65, s65, 0
	s_add_i32 s43, s43, 1
	s_waitcnt lgkmcnt(7)
	v_mfma_i32_32x32x32_i8 v[84:99], v[218:221], v[132:135], v[226:241]
	v_mfma_i32_32x32x32_i8 v[84:99], v[222:225], v[136:139], v[84:99]
	s_waitcnt vmcnt(2) lgkmcnt(0)
	s_barrier
.Lat_u4:
	ds_read_b128 v[108:111], v193
	ds_read_b128 v[112:115], v193 offset:16
	v_mfma_i32_32x32x32_i8 v[84:99], v[242:245], v[140:143], v[84:99]
	ds_read_b128 v[116:119], v195 offset:22528
	ds_read_b128 v[120:123], v196 offset:22528
	s_add_i32 m0, s31, 65536
	s_nop 0
	global_load_lds_dwordx4 v252, s[60:61]
	s_add_i32 m0, s31, 73728
	v_mfma_i32_32x32x32_i8 v[84:99], v[246:249], v[144:147], v[84:99]
	global_load_lds_dwordx4 v254, s[60:61]
	ds_read_b128 v[124:127], v195 offset:20480
	ds_read_b128 v[128:131], v196 offset:20480
	v_mfma_i32_32x32x32_i8 v[84:99], v[202:205], v[148:151], v[84:99]
	ds_read_b128 v[202:205], v195 offset:16384
	v_mfma_i32_32x32x32_i8 v[84:99], v[206:209], v[152:155], v[84:99]
	ds_read_b128 v[206:209], v196 offset:16384
	v_mfma_i32_32x32x32_i8 v[84:99], v[210:213], v[156:159], v[84:99]
	ds_read_b128 v[210:213], v195 offset:18432
	v_mfma_i32_32x32x32_i8 v[84:99], v[214:217], v[160:163], v[84:99]
	ds_read_b128 v[214:217], v196 offset:18432
	v_readlane_b32 s50, v182, s43
	s_waitcnt lgkmcnt(6)
	v_mfma_f32_32x32x64_f8f6f4 v[2:17], v[108:115], v[116:123], v[2:17]
	ds_read_b128 v[218:221], v185
	ds_read_b128 v[222:225], v186
	ds_read_b128 v[242:245], v187
	ds_read_b128 v[246:249], v188
	v_mul_f32_e32 v82, s50, v168
	v_mul_f32_e32 v250, 0x3db8aa3b, v82
	v_fmamk_f32 v251, v250, 0xcb400000, v200
	s_mov_b32 m0, s31
	v_max_i32_e32 v83, v84, v85
	global_load_lds_dwordx4 v255, s[64:65]
	s_add_i32 m0, s31, 8192
	v_max3_i32 v83, v83, v86, v87
	global_load_lds_dwordx4 v201, s[64:65]
	v_max3_i32 v83, v83, v88, v89
	v_max3_i32 v83, v83, v90, v91
	v_max3_i32 v83, v83, v92, v93
	v_max3_i32 v83, v83, v94, v95
	v_max3_i32 v83, v83, v96, v97
	v_max3_i32 v83, v83, v98, v99
	s_waitcnt lgkmcnt(8)
	v_mfma_f32_32x32x64_f8f6f4 v[18:33], v[108:115], v[124:131], v[18:33]
	v_mov_b32_e32 v253, v83
	v_fma_f32 v84, v84, v250, v251
	v_fma_f32 v85, v85, v250, v251
	v_permlane32_swap_b32_e32 v83, v253
	v_fma_f32 v86, v86, v250, v251
	v_fma_f32 v87, v87, v250, v251
	v_max_i32_e32 v83, v83, v253
	v_exp_f32_e32 v84, v84
	v_exp_f32_e32 v85, v85
	v_add_f32_e32 v83, 0xcb400000, v83
	v_exp_f32_e32 v86, v86
	v_exp_f32_e32 v87, v87
	v_fma_f32 v82, v82, v83, -v197
	v_fma_f32 v88, v88, v250, v251
	v_fma_f32 v89, v89, v250, v251
	v_fma_f32 v90, v90, v250, v251
	v_fma_f32 v91, v91, v250, v251
	v_mfma_f32_32x32x64_f8f6f4 v[66:81], v[108:115], v[100:107], v[66:81]
	v_cmp_ge_f32_e64 s[52:53], s42, v82
	v_cvt_pk_fp8_f32 v164, v84, v85
	v_cvt_pk_fp8_f32 v164, v86, v87 op_sel:[0,0,1]
	v_exp_f32_e32 v88, v88
	v_exp_f32_e32 v89, v89
	v_exp_f32_e32 v90, v90
	v_exp_f32_e32 v91, v91
	v_fma_f32 v92, v92, v250, v251
	v_fma_f32 v93, v93, v250, v251
	v_fma_f32 v94, v94, v250, v251
	v_fma_f32 v95, v95, v250, v251
	v_cvt_pk_fp8_f32 v165, v88, v89
	v_cvt_pk_fp8_f32 v165, v90, v91 op_sel:[0,0,1]
	v_exp_f32_e32 v92, v92
	v_exp_f32_e32 v93, v93
	v_exp_f32_e32 v94, v94
	v_exp_f32_e32 v95, v95
	s_waitcnt lgkmcnt(6)
	v_mfma_f32_32x32x64_f8f6f4 v[50:65], v[108:115], v[202:209], v[50:65]
	ds_read_b128 v[202:205], v189
	ds_read_b128 v[206:209], v190
	v_fma_f32 v96, v96, v250, v251
	v_fma_f32 v97, v97, v250, v251
	v_fma_f32 v98, v98, v250, v251
	v_fma_f32 v99, v99, v250, v251
	v_cvt_pk_fp8_f32 v166, v92, v93
	v_cvt_pk_fp8_f32 v166, v94, v95 op_sel:[0,0,1]
	v_exp_f32_e32 v96, v96
	v_exp_f32_e32 v97, v97
	v_exp_f32_e32 v98, v98
	v_exp_f32_e32 v99, v99
	s_cmp_lg_u64 s[52:53], exec
	s_cselect_b32 s1, 1, 0
	s_or_b32 s39, s39, s1
	v_cvt_pk_fp8_f32 v167, v96, v97
	v_cvt_pk_fp8_f32 v167, v98, v99 op_sel:[0,0,1]
	ds_write_b128 v194, v[164:167] offset:8192
	s_waitcnt lgkmcnt(7)
	v_mfma_f32_32x32x64_f8f6f4 v[34:49], v[108:115], v[210:217], v[34:49]
	ds_read_b128 v[210:213], v191
	ds_read_b128 v[214:217], v192
	s_add_u32 s60, s60, 0x4000
	s_addc_u32 s61, s61, 0
	s_add_u32 s64, s64, 0x4000
	s_addc_u32 s65, s65, 0
	s_add_i32 s43, s43, 1
	s_waitcnt lgkmcnt(7)
	v_mfma_i32_32x32x32_i8 v[84:99], v[218:221], v[132:135], v[226:241]
	v_mfma_i32_32x32x32_i8 v[84:99], v[222:225], v[136:139], v[84:99]
	s_waitcnt vmcnt(2) lgkmcnt(0)
	s_barrier
.Lat_u5:
	ds_read_b128 v[108:111], v193 offset:8192
	ds_read_b128 v[112:115], v193 offset:8208
	v_mfma_i32_32x32x32_i8 v[84:99], v[242:245], v[140:143], v[84:99]
	ds_read_b128 v[116:119], v195 offset:38912
	ds_read_b128 v[120:123], v196 offset:38912
	s_cmp_gt_u32 s43, 29
	s_cbranch_scc1 .Lat_nok5
	s_add_i32 m0, s31, 81920
	s_nop 0
	global_load_lds_dwordx4 v252, s[60:61]
	s_add_i32 m0, s31, 90112
	v_mfma_i32_32x32x32_i8 v[84:99], v[246:249], v[144:147], v[84:99]
	global_load_lds_dwordx4 v254, s[60:61]
	s_branch .Lat_k5

.Lat_k5:
	ds_read_b128 v[124:127], v195 offset:36864
	ds_read_b128 v[128:131], v196 offset:36864
	v_mfma_i32_32x32x32_i8 v[84:99], v[202:205], v[148:151], v[84:99]
	ds_read_b128 v[202:205], v195 offset:32768
	v_mfma_i32_32x32x32_i8 v[84:99], v[206:209], v[152:155], v[84:99]
	ds_read_b128 v[206:209], v196 offset:32768
	v_mfma_i32_32x32x32_i8 v[84:99], v[210:213], v[156:159], v[84:99]
	ds_read_b128 v[210:213], v195 offset:34816
	v_mfma_i32_32x32x32_i8 v[84:99], v[214:217], v[160:163], v[84:99]
	ds_read_b128 v[214:217], v196 offset:34816
	v_readlane_b32 s50, v182, s43
	s_waitcnt lgkmcnt(6)
	v_mfma_f32_32x32x64_f8f6f4 v[2:17], v[108:115], v[116:123], v[2:17]
	ds_read_b128 v[218:221], v185 offset:16384
	ds_read_b128 v[222:225], v186 offset:16384
	ds_read_b128 v[242:245], v187 offset:16384
	ds_read_b128 v[246:249], v188 offset:16384
	v_mul_f32_e32 v82, s50, v168
	v_mul_f32_e32 v250, 0x3db8aa3b, v82
	v_fmamk_f32 v251, v250, 0xcb400000, v200
	s_add_i32 m0, s31, 16384
	v_max_i32_e32 v83, v84, v85
	global_load_lds_dwordx4 v255, s[64:65]
	s_add_i32 m0, s31, 24576
	v_max3_i32 v83, v83, v86, v87
	global_load_lds_dwordx4 v201, s[64:65]
	v_max3_i32 v83, v83, v88, v89
	v_max3_i32 v83, v83, v90, v91
	v_max3_i32 v83, v83, v92, v93
	v_max3_i32 v83, v83, v94, v95
	v_max3_i32 v83, v83, v96, v97
	v_max3_i32 v83, v83, v98, v99
	s_waitcnt lgkmcnt(8)
	v_mfma_f32_32x32x64_f8f6f4 v[18:33], v[108:115], v[124:131], v[18:33]
	v_mov_b32_e32 v253, v83
	v_fma_f32 v84, v84, v250, v251
	v_fma_f32 v85, v85, v250, v251
	v_permlane32_swap_b32_e32 v83, v253
	v_fma_f32 v86, v86, v250, v251
	v_fma_f32 v87, v87, v250, v251
	v_max_i32_e32 v83, v83, v253
	v_exp_f32_e32 v84, v84
	v_exp_f32_e32 v85, v85
	v_add_f32_e32 v83, 0xcb400000, v83
	v_exp_f32_e32 v86, v86
	v_exp_f32_e32 v87, v87
	v_fma_f32 v82, v82, v83, -v197
	v_fma_f32 v88, v88, v250, v251
	v_fma_f32 v89, v89, v250, v251
	v_fma_f32 v90, v90, v250, v251
	v_fma_f32 v91, v91, v250, v251
	v_mfma_f32_32x32x64_f8f6f4 v[66:81], v[108:115], v[100:107], v[66:81]
	v_cmp_ge_f32_e64 s[52:53], s42, v82
	v_cvt_pk_fp8_f32 v164, v84, v85
	v_cvt_pk_fp8_f32 v164, v86, v87 op_sel:[0,0,1]
	v_exp_f32_e32 v88, v88
	v_exp_f32_e32 v89, v89
	v_exp_f32_e32 v90, v90
	v_exp_f32_e32 v91, v91
	v_fma_f32 v92, v92, v250, v251
	v_fma_f32 v93, v93, v250, v251
	v_fma_f32 v94, v94, v250, v251
	v_fma_f32 v95, v95, v250, v251
	v_cvt_pk_fp8_f32 v165, v88, v89
	v_cvt_pk_fp8_f32 v165, v90, v91 op_sel:[0,0,1]
	v_exp_f32_e32 v92, v92
	v_exp_f32_e32 v93, v93
	v_exp_f32_e32 v94, v94
	v_exp_f32_e32 v95, v95
	s_waitcnt lgkmcnt(6)
	v_mfma_f32_32x32x64_f8f6f4 v[50:65], v[108:115], v[202:209], v[50:65]
	ds_read_b128 v[202:205], v189 offset:16384
	ds_read_b128 v[206:209], v190 offset:16384
	v_fma_f32 v96, v96, v250, v251
	v_fma_f32 v97, v97, v250, v251
	v_fma_f32 v98, v98, v250, v251
	v_fma_f32 v99, v99, v250, v251
	v_cvt_pk_fp8_f32 v166, v92, v93
	v_cvt_pk_fp8_f32 v166, v94, v95 op_sel:[0,0,1]
	v_exp_f32_e32 v96, v96
	v_exp_f32_e32 v97, v97
	v_exp_f32_e32 v98, v98
	v_exp_f32_e32 v99, v99
	s_cmp_lg_u64 s[52:53], exec
	s_cselect_b32 s1, 1, 0
	s_or_b32 s39, s39, s1
	v_cvt_pk_fp8_f32 v167, v96, v97
	v_cvt_pk_fp8_f32 v167, v98, v99 op_sel:[0,0,1]
	ds_write_b128 v194, v[164:167]
	s_waitcnt lgkmcnt(7)
	v_mfma_f32_32x32x64_f8f6f4 v[34:49], v[108:115], v[210:217], v[34:49]
	ds_read_b128 v[210:213], v191 offset:16384
	ds_read_b128 v[214:217], v192 offset:16384
	s_add_u32 s60, s60, 0x4000
	s_addc_u32 s61, s61, 0
	s_add_u32 s64, s64, 0x4000
	s_addc_u32 s65, s65, 0
	s_add_i32 s43, s43, 1
	s_waitcnt lgkmcnt(7)
	v_mfma_i32_32x32x32_i8 v[84:99], v[218:221], v[132:135], v[226:241]
	v_mfma_i32_32x32x32_i8 v[84:99], v[222:225], v[136:139], v[84:99]
	s_cmp_gt_u32 s43, 30
	s_cbranch_scc1 .Lat_drain
	s_waitcnt vmcnt(2) lgkmcnt(0)
	s_barrier
	s_branch .Lat_u0
.Lat_drain:
	s_waitcnt vmcnt(0) lgkmcnt(0)
	s_barrier
	s_branch .Lat_u0
.Lat_last:
	s_waitcnt vmcnt(0) lgkmcnt(0)
	s_barrier
	v_add_u32_e32 v250, 0xc000, v184
	v_sub_u32_e32 v185, v185, v250
	v_sub_u32_e32 v186, v186, v250
	v_sub_u32_e32 v187, v187, v250
	v_sub_u32_e32 v188, v188, v250
	v_sub_u32_e32 v189, v189, v250
	v_sub_u32_e32 v190, v190, v250
	v_sub_u32_e32 v191, v191, v250
	v_sub_u32_e32 v192, v192, v250

	.amdhsa_kernel _Z11attn_kernelPKhS0_S0_PKfS2_PhPfS4_
		.amdhsa_group_segment_fixed_size 0
		.amdhsa_private_segment_fixed_size 0
		.amdhsa_kernarg_size 64
		.amdhsa_user_sgpr_count 2
		.amdhsa_user_sgpr_dispatch_ptr 0
		.amdhsa_user_sgpr_queue_ptr 0
		.amdhsa_user_sgpr_kernarg_segment_ptr 1
		.amdhsa_user_sgpr_dispatch_id 0
		.amdhsa_user_sgpr_kernarg_preload_length 0
		.amdhsa_user_sgpr_kernarg_preload_offset 0
		.amdhsa_user_sgpr_private_segment_size 0
		.amdhsa_uses_dynamic_stack 0
		.amdhsa_enable_private_segment 0
		.amdhsa_system_sgpr_workgroup_id_x 1
		.amdhsa_system_sgpr_workgroup_id_y 0
		.amdhsa_system_sgpr_workgroup_id_z 0
		.amdhsa_system_sgpr_workgroup_info 0
		.amdhsa_system_vgpr_workitem_id 0
		.amdhsa_next_free_vgpr 256
		.amdhsa_next_free_sgpr 66
		.amdhsa_accum_offset 256
		.amdhsa_reserve_vcc 1
		.amdhsa_float_round_mode_32 0
		.amdhsa_float_round_mode_16_64 0
		.amdhsa_float_denorm_mode_32 3
		.amdhsa_float_denorm_mode_16_64 3
		.amdhsa_dx10_clamp 1
		.amdhsa_ieee_mode 1
		.amdhsa_fp16_overflow 0
		.amdhsa_tg_split 0
		.amdhsa_exception_fp_ieee_invalid_op 0
		.amdhsa_exception_fp_denorm_src 0
		.amdhsa_exception_fp_ieee_div_zero 0
		.amdhsa_exception_fp_ieee_overflow 0
		.amdhsa_exception_fp_ieee_underflow 0
		.amdhsa_exception_fp_ieee_inexact 0
		.amdhsa_exception_int_div_zero 0
	.end_amdhsa_kernel

amdhsa.kernels:
  - .agpr_count:     0
    .args:
      - .actual_access:  read_only
        .address_space:  global
        .offset:         0
        .size:           8
        .value_kind:     global_buffer
      - .actual_access:  read_only
        .address_space:  global
        .offset:         8
        .size:           8
        .value_kind:     global_buffer
      - .actual_access:  read_only
        .address_space:  global
        .offset:         16
        .size:           8
        .value_kind:     global_buffer
      - .actual_access:  write_only
        .address_space:  global
        .offset:         24
        .size:           8
        .value_kind:     global_buffer
      - .actual_access:  write_only
        .address_space:  global
        .offset:         32
        .size:           8
        .value_kind:     global_buffer
      - .actual_access:  write_only
        .address_space:  global
        .offset:         40
        .size:           8
        .value_kind:     global_buffer
    .group_segment_fixed_size: 512
    .kernarg_segment_align: 8
    .kernarg_segment_size: 48
    .language:       OpenCL C
    .language_version:
      - 2
      - 0
    .max_flat_workgroup_size: 1024
    .name:           _Z11prep_kernelPKfS0_S0_PdPtS2_
    .private_segment_fixed_size: 0
    .sgpr_count:     22
    .sgpr_spill_count: 0
    .symbol:         _Z11prep_kernelPKfS0_S0_PdPtS2_.kd
    .uniform_work_group_size: 1
    .uses_dynamic_stack: false
    .vgpr_count:     32
    .vgpr_spill_count: 0
    .wavefront_size: 64
  - .agpr_count:     0
    .args:
      - .actual_access:  read_only
        .address_space:  global
        .offset:         0
        .size:           8
        .value_kind:     global_buffer
      - .actual_access:  read_only
        .address_space:  global
        .offset:         8
        .size:           8
        .value_kind:     global_buffer
      - .actual_access:  read_only
        .address_space:  global
        .offset:         16
        .size:           8
        .value_kind:     global_buffer
      - .actual_access:  read_only
        .address_space:  global
        .offset:         24
        .size:           8
        .value_kind:     global_buffer
      - .actual_access:  read_only
        .address_space:  global
        .offset:         32
        .size:           8
        .value_kind:     global_buffer
      - .actual_access:  read_only
        .address_space:  global
        .offset:         40
        .size:           8
        .value_kind:     global_buffer
      - .actual_access:  write_only
        .address_space:  global
        .offset:         48
        .size:           8
        .value_kind:     global_buffer
      - .actual_access:  write_only
        .address_space:  global
        .offset:         56
        .size:           8
        .value_kind:     global_buffer
      - .actual_access:  write_only
        .address_space:  global
        .offset:         64
        .size:           8
        .value_kind:     global_buffer
    .group_segment_fixed_size: 0
    .kernarg_segment_align: 8
    .kernarg_segment_size: 72
    .language:       OpenCL C
    .language_version:
      - 2
      - 0
    .max_flat_workgroup_size: 512
    .name:           _Z10qkv_kernelPKfS0_S0_PKdPKtS0_PhPfS6_
    .private_segment_fixed_size: 0
    .sgpr_count:     30
    .sgpr_spill_count: 0
    .symbol:         _Z10qkv_kernelPKfS0_S0_PKdPKtS0_PhPfS6_.kd
    .uniform_work_group_size: 1
    .uses_dynamic_stack: false
    .vgpr_count:     182
    .vgpr_spill_count: 0
    .wavefront_size: 64
  - .agpr_count:     0
    .args:
      - .actual_access:  read_only
        .address_space:  global
        .offset:         0
        .size:           8
        .value_kind:     global_buffer
      - .address_space:  global
        .offset:         8
        .size:           8
        .value_kind:     global_buffer
      - .address_space:  global
        .offset:         16
        .size:           8
        .value_kind:     global_buffer
      - .actual_access:  read_only
        .address_space:  global
        .offset:         24
        .size:           8
        .value_kind:     global_buffer
      - .actual_access:  read_only
        .address_space:  global
        .offset:         32
        .size:           8
        .value_kind:     global_buffer
      - .actual_access:  write_only
        .address_space:  global
        .offset:         40
        .size:           8
        .value_kind:     global_buffer
      - .actual_access:  write_only
        .address_space:  global
        .offset:         48
        .size:           8
        .value_kind:     global_buffer
      - .actual_access:  write_only
        .address_space:  global
        .offset:         56
        .size:           8
        .value_kind:     global_buffer
    .group_segment_fixed_size: 0
    .kernarg_segment_align: 8
    .kernarg_segment_size: 64
    .language:       OpenCL C
    .language_version:
      - 2
      - 0
    .max_flat_workgroup_size: 512
    .name:           _Z11attn_kernelPKhS0_S0_PKfS2_PhPfS4_
    .private_segment_fixed_size: 0
    .sgpr_count:     72
    .sgpr_spill_count: 0
    .symbol:         _Z11attn_kernelPKhS0_S0_PKfS2_PhPfS4_.kd
    .uniform_work_group_size: 1
    .uses_dynamic_stack: false
    .vgpr_count:     256
    .vgpr_spill_count: 0
    .wavefront_size: 64
  - .agpr_count:     0
    .args:
      - .actual_access:  read_only
        .address_space:  global
        .offset:         0
        .size:           8
        .value_kind:     global_buffer
      - .actual_access:  read_only
        .address_space:  global
        .offset:         8
        .size:           8
        .value_kind:     global_buffer
      - .actual_access:  read_only
        .address_space:  global
        .offset:         16
        .size:           8
        .value_kind:     global_buffer
      - .actual_access:  read_only
        .address_space:  global
        .offset:         24
        .size:           8
        .value_kind:     global_buffer
      - .actual_access:  read_only
        .address_space:  global
        .offset:         32
        .size:           8
        .value_kind:     global_buffer
      - .actual_access:  read_only
        .address_space:  global
        .offset:         40
        .size:           8
        .value_kind:     global_buffer
      - .actual_access:  write_only
        .address_space:  global
        .offset:         48
        .size:           8
        .value_kind:     global_buffer
    .group_segment_fixed_size: 16640
    .kernarg_segment_align: 8
    .kernarg_segment_size: 56
    .language:       OpenCL C
    .language_version:
      - 2
      - 0
    .max_flat_workgroup_size: 512
    .name:           _Z14outproj_kernelPKhPKfS2_PKtS2_S2_Pf
    .private_segment_fixed_size: 0
    .sgpr_count:     24
    .sgpr_spill_count: 0
    .symbol:         _Z14outproj_kernelPKhPKfS2_PKtS2_S2_Pf.kd
    .uniform_work_group_size: 1
    .uses_dynamic_stack: false
    .vgpr_count:     109
    .vgpr_spill_count: 0
    .wavefront_size: 64
